# expert gate/up GEMM: next unit row-table loads issued one K-iteration early (no full DMA drain per unit)
# speedup vs baseline: 1.0308x; 1.0039x over previous
; template <class Epi, class Sched, bool GATHER, bool F8 = false>
; __device__ __forceinline__ void gemm_phase(LAS unsigned char* lds, const Gemm g, const Sched& S, const Epi& E, const int tid) {
;     ...
;         for (int t = 0; t < nt; t += 2) {
;             const bool last = (t == nt - 2);
;             int to = t; asm volatile("" : "+s"(to));
;             const size_t k1 = (size_t)(to + 1) * kstep, k2 = last ? 0 : (size_t)(to + 2) * kstep, k3 = k2 + kstep;
;             const char* b2 = last ? nB : cB + (size_t)(to + 2) * kstep; const char* b3 = b2 + kstep;
;             const char* a2p = last ? nA : cA;
;             if constexpr (GATHER) { if (last) { if (has_next) { PG8_AOFF(on, nxt); } else {
; #pragma unroll
;                 for (int h = 0; h < 2; ++h)
; #pragma unroll
;                     for (int i = 0; i < 2; ++i) on[h][i] = oc[h][i]; } } }
.LBB0_1271:
	s_mov_b32 s38, s75
	s_add_i32 s75, s75, 2
	s_cmp_eq_u32 s38, 10
	s_cbranch_scc0 .Lm1_nopf
	s_andn2_b64 vcc, exec, s[48:49]
	s_cbranch_vccnz .Lm1_nopf
	v_mov_b32_e32 v2, v1
	s_nop 0
	v_ashrrev_i32_e32 v3, 31, v2
	v_lshrrev_b32_e32 v3, 26, v3
	v_lshlrev_b32_e32 v6, 4, v2
	v_add_u32_e32 v7, v2, v3
	v_bfe_i32 v2, v2, 27, 1
	v_lshrrev_b32_e32 v2, 22, v2
	v_add_u32_e32 v2, v6, v2
	v_and_b32_e32 v2, 0xfffffc00, v2
	v_sub_u32_e32 v2, v6, v2
	v_lshrrev_b32_e32 v4, 5, v2
	v_ashrrev_i32_e32 v3, 6, v7
	v_bitop3_b32 v8, v4, v2, 16 bitop3:0x6c
	v_lshlrev_b32_e32 v2, 3, v3
	v_ashrrev_i32_e32 v3, 31, v8
	v_lshrrev_b32_e32 v3, 26, v3
	v_add_u32_e32 v9, v8, v3
	v_and_b32_e32 v2, -16, v2
	v_ashrrev_i32_e32 v3, 6, v9
	v_add3_u32 v2, v2, v249, v3
	v_ashrrev_i32_e32 v3, 31, v2
	v_lshl_add_u64 v[4:5], v[2:3], 2, s[16:17]
	v_add_u32_e32 v2, 0x80, v2
	v_ashrrev_i32_e32 v3, 31, v2
	v_lshl_add_u64 v[2:3], v[2:3], 2, s[16:17]
	global_load_dword v242, v[4:5], off
	global_load_dword v243, v[2:3], off
	v_add_u32_e32 v2, 0x2000, v6
	v_ashrrev_i32_e32 v3, 31, v2
	v_lshrrev_b32_e32 v3, 22, v3
	v_add_u32_e32 v3, v2, v3
	v_ashrrev_i32_e32 v6, 10, v3
	v_mul_i32_i24_e32 v3, 0x400, v6
	v_sub_u32_e32 v2, v2, v3
	v_lshrrev_b32_e32 v3, 5, v2
	v_bitop3_b32 v12, v3, v2, 16 bitop3:0x6c
	v_ashrrev_i32_e32 v3, 31, v12
	v_lshrrev_b32_e32 v3, 26, v3
	v_lshlrev_b32_e32 v2, 3, v6
	v_add_u32_e32 v13, v12, v3
	v_and_b32_e32 v2, -16, v2
	v_ashrrev_i32_e32 v3, 6, v13
	v_add3_u32 v2, v2, v249, v3
	v_ashrrev_i32_e32 v3, 31, v2
	v_lshl_add_u64 v[4:5], v[2:3], 2, s[16:17]
	v_add_u32_e32 v2, 0x80, v2
	v_ashrrev_i32_e32 v3, 31, v2
	v_lshl_add_u64 v[2:3], v[2:3], 2, s[16:17]
	global_load_dword v244, v[4:5], off
	s_nop 0
	global_load_dword v245, v[2:3], off
	v_lshlrev_b32_e32 v5, 6, v6
	v_and_b32_e32 v6, 0xffffffc0, v9
	v_and_b32_e32 v3, 64, v7
	v_sub_u32_e32 v6, v8, v6
	v_add_u32_e32 v3, v6, v3
	v_and_b32_e32 v6, 0xffffffc0, v13
	v_and_b32_e32 v5, 64, v5
	v_sub_u32_e32 v6, v12, v6
	v_add_u32_e32 v5, v6, v5
	v_mov_b32_e32 v250, v3
	v_mov_b32_e32 v251, v5
.Lm1_nopf:
	s_cmp_eq_u32 s38, 12
	s_cselect_b64 s[34:35], -1, 0
	s_cmp_lg_u32 s38, 12
	s_cselect_b64 s[54:55], -1, 0
	s_mov_b32 s38, s75
	s_and_b64 vcc, exec, s[54:55]
	s_cbranch_vccnz .LBB0_1274
	s_andn2_b64 vcc, exec, s[48:49]
	v_mov_b32_e32 v246, v204
	v_mov_b32_e32 v200, v208
	v_mov_b32_e32 v247, v206
	v_mov_b32_e32 v202, v210
	s_cbranch_vccnz .LBB0_1274
	s_waitcnt vmcnt(16)
	v_max_i32_e32 v6, 0, v242
	v_lshl_add_u32 v246, v6, 11, v250
	v_max_i32_e32 v6, 0, v243
	v_lshl_add_u32 v247, v6, 11, v250
	v_max_i32_e32 v3, 0, v244
	v_lshl_add_u32 v200, v3, 11, v251
	v_max_i32_e32 v2, 0, v245
	v_lshl_add_u32 v202, v2, 11, v251
